# v59 + GQA fast-path P.V: each MFMA waits only for the two transposed V reads it consumes (counted lgkmcnt) instead of a full drain per group; full drain kept before the buffer-reuse barrier
# baseline (speedup 1.0000x reference)
.LBB0_881:
	ds_read_b128 v[96:99], v216 offset:49152
	ds_read_b128 v[100:103], v216 offset:57344
	ds_read_b128 v[178:181], v218 offset:49152
	ds_read_b128 v[182:185], v218 offset:57344
	ds_read_b128 v[240:243], v219 offset:49152
	ds_read_b128 v[244:247], v219 offset:57344
	v_add_f32_e32 v88, v64, v65
	v_add_f32_e32 v89, v72, v73
	v_add_f32_e32 v90, v80, v81
	v_add_f32_e32 v91, v194, v195
	v_add_f32_e32 v88, v66, v88
	v_add_f32_e32 v89, v74, v89
	v_add_f32_e32 v90, v82, v90
	s_waitcnt lgkmcnt(4)
	v_mfma_f32_32x32x16_bf16 v[112:127], v[96:99], v[138:141], 0
	v_mfma_f32_32x32x16_bf16 v[96:111], v[100:103], v[138:141], 0
	v_add_f32_e32 v91, v196, v91
	v_add_f32_e32 v88, v67, v88
	v_add_f32_e32 v89, v75, v89
	v_add_f32_e32 v90, v83, v90
	v_add_f32_e32 v91, v197, v91
	v_add_f32_e32 v88, v68, v88
	v_add_f32_e32 v89, v76, v89
	s_waitcnt lgkmcnt(2)
	v_mfma_f32_32x32x16_bf16 v[112:127], v[178:181], v[154:157], v[112:127]
	v_mfma_f32_32x32x16_bf16 v[96:111], v[182:185], v[154:157], v[96:111]
	ds_read_b128 v[178:181], v220 offset:49152
	ds_read_b128 v[182:185], v220 offset:57344
	v_add_f32_e32 v90, v84, v90
	v_add_f32_e32 v91, v92, v91
	v_add_f32_e32 v88, v69, v88
	v_add_f32_e32 v89, v77, v89
	v_add_f32_e32 v90, v85, v90
	v_add_f32_e32 v91, v93, v91
	v_add_f32_e32 v88, v70, v88
	s_waitcnt lgkmcnt(2)
	v_mfma_f32_32x32x16_bf16 v[112:127], v[240:243], v[158:161], v[112:127]
	v_mfma_f32_32x32x16_bf16 v[96:111], v[244:247], v[158:161], v[96:111]
	ds_read_b128 v[240:243], v221 offset:49152
	ds_read_b128 v[244:247], v221 offset:57344
	v_add_f32_e32 v89, v78, v89
	v_add_f32_e32 v90, v86, v90
	v_add_f32_e32 v91, v94, v91
	v_add_f32_e32 v88, v71, v88
	v_add_f32_e32 v89, v79, v89
	v_add_f32_e32 v90, v87, v90
	v_add_f32_e32 v91, v95, v91
	s_waitcnt lgkmcnt(2)
	v_mfma_f32_32x32x16_bf16 v[112:127], v[178:181], v[150:153], v[112:127]
	v_mfma_f32_32x32x16_bf16 v[96:111], v[182:185], v[150:153], v[96:111]
	ds_read_b128 v[178:181], v222 offset:49152
	ds_read_b128 v[182:185], v222 offset:57344
	v_add_f32_e32 v88, v89, v88
	v_add_f32_e32 v89, v91, v90
	v_add_f32_e32 v227, v88, v89
	v_cvt_pk_bf16_f32 v88, v64, v65
	v_cvt_pk_bf16_f32 v89, v66, v67
	v_cvt_pk_bf16_f32 v90, v68, v69
	v_cvt_pk_bf16_f32 v91, v70, v71
	s_waitcnt lgkmcnt(2)
	v_mfma_f32_32x32x16_bf16 v[112:127], v[240:243], v[146:149], v[112:127]
	v_mfma_f32_32x32x16_bf16 v[96:111], v[244:247], v[146:149], v[96:111]
	ds_read_b128 v[240:243], v224 offset:49152
	ds_read_b128 v[244:247], v224 offset:57344
	v_cvt_pk_bf16_f32 v72, v72, v73
	v_cvt_pk_bf16_f32 v73, v74, v75
	v_cvt_pk_bf16_f32 v74, v76, v77
	v_cvt_pk_bf16_f32 v75, v78, v79
	s_waitcnt lgkmcnt(2)
	v_mfma_f32_32x32x16_bf16 v[112:127], v[178:181], v[142:145], v[112:127]
	v_mfma_f32_32x32x16_bf16 v[96:111], v[182:185], v[142:145], v[96:111]
	ds_read_b128 v[178:181], v223 offset:49152
	ds_read_b128 v[182:185], v223 offset:57344
	v_cvt_pk_bf16_f32 v64, v80, v81
	v_cvt_pk_bf16_f32 v65, v82, v83
	v_cvt_pk_bf16_f32 v66, v84, v85
	v_cvt_pk_bf16_f32 v67, v86, v87
	v_cvt_pk_bf16_f32 v68, v194, v195
	v_cvt_pk_bf16_f32 v69, v196, v197
	v_cvt_pk_bf16_f32 v70, v92, v93
	s_waitcnt lgkmcnt(2)
	v_mfma_f32_32x32x16_bf16 v[112:127], v[240:243], v[134:137], v[112:127]
	v_mfma_f32_32x32x16_bf16 v[96:111], v[244:247], v[134:137], v[96:111]
	v_cvt_pk_bf16_f32 v71, v94, v95
	s_waitcnt lgkmcnt(0)
	v_mfma_f32_32x32x16_bf16 v[112:127], v[178:181], v[130:133], v[112:127]
	v_mfma_f32_32x32x16_bf16 v[96:111], v[182:185], v[130:133], v[96:111]
	s_add_i32 s2, s39, -1
	s_mul_i32 s2, s2, s62
	s_lshl_b32 s72, s2, 6
	s_lshl_b64 s[2:3], s[72:73], 1
	s_add_u32 s12, s10, s2
	s_addc_u32 s13, s11, s3
	s_add_u32 s2, s8, s2
	s_addc_u32 s3, s9, s3
	global_load_dwordx4 v[178:181], v128, s[12:13]
	global_load_dwordx4 v[182:185], v198, s[12:13]
	global_load_dwordx4 v[186:189], v128, s[2:3]
	global_load_dwordx4 v[190:193], v198, s[2:3]
	ds_read_b64_tr_b16 v[76:77], v209 offset:0
	ds_read_b64_tr_b16 v[78:79], v209 offset:0x800
	ds_read_b64_tr_b16 v[80:81], v209 offset:0x1000
	ds_read_b64_tr_b16 v[82:83], v209 offset:0x1800
	ds_read_b64_tr_b16 v[84:85], v209 offset:0x2000
	ds_read_b64_tr_b16 v[86:87], v209 offset:0x2800
	ds_read_b64_tr_b16 v[92:93], v209 offset:0x3000
	ds_read_b64_tr_b16 v[94:95], v209 offset:0x3800
	s_nop 0
	s_waitcnt lgkmcnt(6)
	v_mfma_f32_32x32x16_bf16 v[0:15], v[76:79], v[88:91], v[0:15]
	s_waitcnt lgkmcnt(4)
	v_mfma_f32_32x32x16_bf16 v[0:15], v[80:83], v[72:75], v[0:15]
	s_waitcnt lgkmcnt(2)
	v_mfma_f32_32x32x16_bf16 v[0:15], v[84:87], v[64:67], v[0:15]
	ds_read_b64_tr_b16 v[76:77], v209 offset:0x200
	ds_read_b64_tr_b16 v[78:79], v209 offset:0xa00
	ds_read_b64_tr_b16 v[80:81], v209 offset:0x1200
	s_waitcnt lgkmcnt(3)
	v_mfma_f32_32x32x16_bf16 v[0:15], v[92:95], v[68:71], v[0:15]
	ds_read_b64_tr_b16 v[82:83], v209 offset:0x1a00
	ds_read_b64_tr_b16 v[84:85], v209 offset:0x2200
	ds_read_b64_tr_b16 v[86:87], v209 offset:0x2a00
	ds_read_b64_tr_b16 v[92:93], v209 offset:0x3200
	ds_read_b64_tr_b16 v[94:95], v209 offset:0x3a00
	s_waitcnt lgkmcnt(6)
	v_mfma_f32_32x32x16_bf16 v[48:63], v[76:79], v[88:91], v[48:63]
	s_waitcnt lgkmcnt(4)
	v_mfma_f32_32x32x16_bf16 v[48:63], v[80:83], v[72:75], v[48:63]
	s_waitcnt lgkmcnt(2)
	v_mfma_f32_32x32x16_bf16 v[48:63], v[84:87], v[64:67], v[48:63]
	ds_read_b64_tr_b16 v[76:77], v209 offset:0x400
	ds_read_b64_tr_b16 v[78:79], v209 offset:0xc00
	ds_read_b64_tr_b16 v[80:81], v209 offset:0x1400
	ds_read_b64_tr_b16 v[82:83], v209 offset:0x1c00
	s_waitcnt lgkmcnt(4)
	v_mfma_f32_32x32x16_bf16 v[48:63], v[92:95], v[68:71], v[48:63]
	ds_read_b64_tr_b16 v[84:85], v209 offset:0x2400
	ds_read_b64_tr_b16 v[86:87], v209 offset:0x2c00
	ds_read_b64_tr_b16 v[92:93], v209 offset:0x3400
	ds_read_b64_tr_b16 v[94:95], v209 offset:0x3c00
	s_waitcnt lgkmcnt(6)
	v_mfma_f32_32x32x16_bf16 v[32:47], v[76:79], v[88:91], v[32:47]
	ds_read_b64_tr_b16 v[76:77], v209 offset:0x600
	ds_read_b64_tr_b16 v[78:79], v209 offset:0xe00
	v_exp_f32_e32 v234, v104
	v_exp_f32_e32 v235, v105
	v_exp_f32_e32 v236, v106
	v_exp_f32_e32 v237, v107
	v_exp_f32_e32 v238, v108
	v_exp_f32_e32 v239, v109
	v_exp_f32_e32 v231, v110
	v_exp_f32_e32 v249, v111
	s_waitcnt lgkmcnt(6)
	v_mfma_f32_32x32x16_bf16 v[32:47], v[80:83], v[72:75], v[32:47]
	v_exp_f32_e32 v80, v112
	v_exp_f32_e32 v81, v113
	v_exp_f32_e32 v82, v114
	v_exp_f32_e32 v83, v115
	s_waitcnt lgkmcnt(4)
	v_mfma_f32_32x32x16_bf16 v[32:47], v[84:87], v[64:67], v[32:47]
	v_exp_f32_e32 v84, v116
	v_exp_f32_e32 v85, v117
	v_exp_f32_e32 v86, v118
	v_exp_f32_e32 v87, v119
	v_exp_f32_e32 v112, v96
	v_exp_f32_e32 v113, v97
	v_exp_f32_e32 v114, v98
	v_exp_f32_e32 v115, v99
	v_exp_f32_e32 v116, v100
	v_exp_f32_e32 v117, v101
	v_exp_f32_e32 v118, v102
	v_exp_f32_e32 v119, v103
	s_waitcnt lgkmcnt(2)
	v_mfma_f32_32x32x16_bf16 v[32:47], v[92:95], v[68:71], v[32:47]
	ds_read_b64_tr_b16 v[92:93], v209 offset:0x1600
	ds_read_b64_tr_b16 v[94:95], v209 offset:0x1e00
	ds_read_b64_tr_b16 v[96:97], v209 offset:0x2600
	ds_read_b64_tr_b16 v[98:99], v209 offset:0x2e00
	ds_read_b64_tr_b16 v[100:101], v209 offset:0x3600
	ds_read_b64_tr_b16 v[102:103], v209 offset:0x3e00
	s_waitcnt lgkmcnt(6)
	v_mfma_f32_32x32x16_bf16 v[16:31], v[76:79], v[88:91], v[16:31]
	v_exp_f32_e32 v88, v120
	v_exp_f32_e32 v89, v121
	v_exp_f32_e32 v90, v122
	v_exp_f32_e32 v91, v123
	s_waitcnt lgkmcnt(4)
	v_mfma_f32_32x32x16_bf16 v[16:31], v[92:95], v[72:75], v[16:31]
	v_exp_f32_e32 v92, v124
	v_exp_f32_e32 v93, v125
	v_exp_f32_e32 v94, v126
	v_exp_f32_e32 v95, v127
	s_waitcnt lgkmcnt(0)
	s_barrier
	v_mfma_f32_32x32x16_bf16 v[16:31], v[96:99], v[64:67], v[16:31]
	s_waitcnt vmcnt(4)
	ds_write_b128 v212, v[162:165]
	ds_write_b128 v213, v[166:169]
	ds_write_b128 v214, v[170:173] offset:32768
	ds_write_b128 v215, v[174:177] offset:32768
	v_mfma_f32_32x32x16_bf16 v[16:31], v[100:103], v[68:71], v[16:31]
.LBB0_883:
	s_waitcnt lgkmcnt(0)
	s_barrier
	ds_read_b128 v[64:67], v216 offset:32768
	ds_read_b128 v[68:71], v216 offset:40960
	ds_read_b128 v[162:165], v218 offset:32768
	ds_read_b128 v[166:169], v218 offset:40960
	ds_read_b128 v[240:243], v219 offset:32768
	ds_read_b128 v[244:247], v219 offset:40960
	v_add_f32_e32 v120, v80, v81
	v_add_f32_e32 v121, v88, v89
	v_add_f32_e32 v122, v112, v113
	v_add_f32_e32 v123, v234, v235
	v_add_f32_e32 v120, v82, v120
	v_add_f32_e32 v121, v90, v121
	v_add_f32_e32 v122, v114, v122
	s_waitcnt lgkmcnt(4)
	v_mfma_f32_32x32x16_bf16 v[96:111], v[64:67], v[138:141], 0
	v_mfma_f32_32x32x16_bf16 v[64:79], v[68:71], v[138:141], 0
	v_add_f32_e32 v123, v236, v123
	v_add_f32_e32 v120, v83, v120
	v_add_f32_e32 v121, v91, v121
	v_add_f32_e32 v122, v115, v122
	v_add_f32_e32 v123, v237, v123
	v_add_f32_e32 v120, v84, v120
	v_add_f32_e32 v121, v92, v121
	s_waitcnt lgkmcnt(2)
	v_mfma_f32_32x32x16_bf16 v[96:111], v[162:165], v[154:157], v[96:111]
	v_mfma_f32_32x32x16_bf16 v[64:79], v[166:169], v[154:157], v[64:79]
	ds_read_b128 v[162:165], v220 offset:32768
	ds_read_b128 v[166:169], v220 offset:40960
	v_add_f32_e32 v122, v116, v122
	v_add_f32_e32 v123, v238, v123
	v_add_f32_e32 v120, v85, v120
	v_add_f32_e32 v121, v93, v121
	v_add_f32_e32 v122, v117, v122
	v_add_f32_e32 v123, v239, v123
	v_add_f32_e32 v120, v86, v120
	s_waitcnt lgkmcnt(2)
	v_mfma_f32_32x32x16_bf16 v[96:111], v[240:243], v[158:161], v[96:111]
	v_mfma_f32_32x32x16_bf16 v[64:79], v[244:247], v[158:161], v[64:79]
	ds_read_b128 v[240:243], v221 offset:32768
	ds_read_b128 v[244:247], v221 offset:40960
	v_add_f32_e32 v121, v94, v121
	v_add_f32_e32 v122, v118, v122
	v_add_f32_e32 v123, v231, v123
	v_add_f32_e32 v120, v87, v120
	v_add_f32_e32 v121, v95, v121
	v_add_f32_e32 v122, v119, v122
	v_add_f32_e32 v123, v249, v123
	s_waitcnt lgkmcnt(2)
	v_mfma_f32_32x32x16_bf16 v[96:111], v[162:165], v[150:153], v[96:111]
	v_mfma_f32_32x32x16_bf16 v[64:79], v[166:169], v[150:153], v[64:79]
	ds_read_b128 v[162:165], v222 offset:32768
	ds_read_b128 v[166:169], v222 offset:40960
	v_add_f32_e32 v120, v121, v120
	v_add_f32_e32 v121, v123, v122
	v_add_f32_e32 v229, v120, v121
	v_cvt_pk_bf16_f32 v124, v80, v81
	v_cvt_pk_bf16_f32 v125, v82, v83
	v_cvt_pk_bf16_f32 v126, v84, v85
	s_waitcnt lgkmcnt(2)
	v_mfma_f32_32x32x16_bf16 v[96:111], v[240:243], v[146:149], v[96:111]
	v_mfma_f32_32x32x16_bf16 v[64:79], v[244:247], v[146:149], v[64:79]
	ds_read_b128 v[240:243], v224 offset:32768
	ds_read_b128 v[244:247], v224 offset:40960
	v_cvt_pk_bf16_f32 v127, v86, v87
	v_cvt_pk_bf16_f32 v120, v88, v89
	v_cvt_pk_bf16_f32 v121, v90, v91
	v_cvt_pk_bf16_f32 v122, v92, v93
	v_cvt_pk_bf16_f32 v123, v94, v95
	v_cvt_pk_bf16_f32 v112, v112, v113
	v_cvt_pk_bf16_f32 v113, v114, v115
	s_waitcnt lgkmcnt(2)
	v_mfma_f32_32x32x16_bf16 v[96:111], v[162:165], v[142:145], v[96:111]
	v_mfma_f32_32x32x16_bf16 v[64:79], v[166:169], v[142:145], v[64:79]
	ds_read_b128 v[162:165], v223 offset:32768
	ds_read_b128 v[166:169], v223 offset:40960
	v_cvt_pk_bf16_f32 v114, v116, v117
	v_cvt_pk_bf16_f32 v115, v118, v119
	v_cvt_pk_bf16_f32 v116, v234, v235
	v_cvt_pk_bf16_f32 v117, v236, v237
	v_cvt_pk_bf16_f32 v118, v238, v239
	v_cvt_pk_bf16_f32 v119, v231, v249
	s_waitcnt lgkmcnt(2)
	v_mfma_f32_32x32x16_bf16 v[96:111], v[240:243], v[134:137], v[96:111]
	v_mfma_f32_32x32x16_bf16 v[64:79], v[244:247], v[134:137], v[64:79]
	s_waitcnt lgkmcnt(0)
	v_mfma_f32_32x32x16_bf16 v[96:111], v[162:165], v[130:133], v[96:111]
	v_mfma_f32_32x32x16_bf16 v[64:79], v[166:169], v[130:133], v[64:79]
	s_min_i32 s2, s39, s14
	s_mul_i32 s2, s2, s62
	s_lshl_b32 s72, s2, 6
	s_lshl_b64 s[2:3], s[72:73], 1
	s_add_u32 s12, s10, s2
	s_addc_u32 s13, s11, s3
	s_add_u32 s2, s8, s2
	s_addc_u32 s3, s9, s3
	global_load_dwordx4 v[162:165], v128, s[12:13]
	global_load_dwordx4 v[166:169], v198, s[12:13]
	global_load_dwordx4 v[170:173], v128, s[2:3]
	global_load_dwordx4 v[174:177], v198, s[2:3]
	ds_read_b64_tr_b16 v[80:81], v211 offset:0
	ds_read_b64_tr_b16 v[82:83], v211 offset:0x800
	ds_read_b64_tr_b16 v[84:85], v211 offset:0x1000
	ds_read_b64_tr_b16 v[86:87], v211 offset:0x1800
	ds_read_b64_tr_b16 v[88:89], v211 offset:0x2000
	ds_read_b64_tr_b16 v[90:91], v211 offset:0x2800
	ds_read_b64_tr_b16 v[92:93], v211 offset:0x3000
	ds_read_b64_tr_b16 v[94:95], v211 offset:0x3800
	s_nop 0
	s_waitcnt lgkmcnt(6)
	v_mfma_f32_32x32x16_bf16 v[0:15], v[80:83], v[124:127], v[0:15]
	s_waitcnt lgkmcnt(4)
	v_mfma_f32_32x32x16_bf16 v[0:15], v[84:87], v[120:123], v[0:15]
	s_waitcnt lgkmcnt(2)
	v_mfma_f32_32x32x16_bf16 v[0:15], v[88:91], v[112:115], v[0:15]
	ds_read_b64_tr_b16 v[80:81], v211 offset:0x200
	ds_read_b64_tr_b16 v[82:83], v211 offset:0xa00
	ds_read_b64_tr_b16 v[84:85], v211 offset:0x1200
	s_waitcnt lgkmcnt(3)
	v_mfma_f32_32x32x16_bf16 v[0:15], v[92:95], v[116:119], v[0:15]
	ds_read_b64_tr_b16 v[86:87], v211 offset:0x1a00
	ds_read_b64_tr_b16 v[88:89], v211 offset:0x2200
	ds_read_b64_tr_b16 v[90:91], v211 offset:0x2a00
	ds_read_b64_tr_b16 v[92:93], v211 offset:0x3200
	ds_read_b64_tr_b16 v[94:95], v211 offset:0x3a00
	s_waitcnt lgkmcnt(6)
	v_mfma_f32_32x32x16_bf16 v[48:63], v[80:83], v[124:127], v[48:63]
	s_waitcnt lgkmcnt(4)
	v_mfma_f32_32x32x16_bf16 v[48:63], v[84:87], v[120:123], v[48:63]
	s_waitcnt lgkmcnt(2)
	v_mfma_f32_32x32x16_bf16 v[48:63], v[88:91], v[112:115], v[48:63]
	ds_read_b64_tr_b16 v[80:81], v211 offset:0x400
	ds_read_b64_tr_b16 v[82:83], v211 offset:0xc00
	ds_read_b64_tr_b16 v[84:85], v211 offset:0x1400
	ds_read_b64_tr_b16 v[86:87], v211 offset:0x1c00
	s_waitcnt lgkmcnt(4)
	v_mfma_f32_32x32x16_bf16 v[48:63], v[92:95], v[116:119], v[48:63]
	ds_read_b64_tr_b16 v[88:89], v211 offset:0x2400
	ds_read_b64_tr_b16 v[90:91], v211 offset:0x2c00
	ds_read_b64_tr_b16 v[92:93], v211 offset:0x3400
	ds_read_b64_tr_b16 v[94:95], v211 offset:0x3c00
	s_waitcnt lgkmcnt(6)
	v_mfma_f32_32x32x16_bf16 v[32:47], v[80:83], v[124:127], v[32:47]
	v_exp_f32_e32 v80, v64
	v_exp_f32_e32 v81, v65
	v_exp_f32_e32 v64, v96
	v_exp_f32_e32 v65, v97
	v_exp_f32_e32 v82, v66
	v_exp_f32_e32 v83, v67
	v_exp_f32_e32 v66, v98
	v_exp_f32_e32 v67, v99
	s_waitcnt lgkmcnt(4)
	v_mfma_f32_32x32x16_bf16 v[32:47], v[84:87], v[120:123], v[32:47]
	v_exp_f32_e32 v84, v68
	v_exp_f32_e32 v85, v69
	v_exp_f32_e32 v68, v100
	v_exp_f32_e32 v69, v101
	v_exp_f32_e32 v86, v70
	v_exp_f32_e32 v87, v71
	v_exp_f32_e32 v70, v102
	v_exp_f32_e32 v71, v103
	s_waitcnt lgkmcnt(2)
	v_mfma_f32_32x32x16_bf16 v[32:47], v[88:91], v[112:115], v[32:47]
	v_exp_f32_e32 v194, v72
	v_exp_f32_e32 v195, v73
	ds_read_b64_tr_b16 v[72:73], v211 offset:0x600
	v_exp_f32_e32 v196, v74
	v_exp_f32_e32 v197, v75
	ds_read_b64_tr_b16 v[74:75], v211 offset:0xe00
	s_waitcnt lgkmcnt(2)
	v_mfma_f32_32x32x16_bf16 v[32:47], v[92:95], v[116:119], v[32:47]
	v_exp_f32_e32 v92, v76
	v_exp_f32_e32 v93, v77
	ds_read_b64_tr_b16 v[76:77], v211 offset:0x1600
	v_exp_f32_e32 v94, v78
	v_exp_f32_e32 v95, v79
	ds_read_b64_tr_b16 v[78:79], v211 offset:0x1e00
	ds_read_b64_tr_b16 v[96:97], v211 offset:0x2600
	ds_read_b64_tr_b16 v[98:99], v211 offset:0x2e00
	ds_read_b64_tr_b16 v[100:101], v211 offset:0x3600
	ds_read_b64_tr_b16 v[102:103], v211 offset:0x3e00
	s_waitcnt lgkmcnt(6)
	v_mfma_f32_32x32x16_bf16 v[16:31], v[72:75], v[124:127], v[16:31]
	v_exp_f32_e32 v72, v104
	v_exp_f32_e32 v73, v105
	v_exp_f32_e32 v74, v106
	v_exp_f32_e32 v75, v107
	s_waitcnt lgkmcnt(4)
	v_mfma_f32_32x32x16_bf16 v[16:31], v[76:79], v[120:123], v[16:31]
	v_exp_f32_e32 v76, v108
	v_exp_f32_e32 v77, v109
	v_exp_f32_e32 v78, v110
	v_exp_f32_e32 v79, v111
	s_waitcnt lgkmcnt(0)
	s_barrier
	v_mfma_f32_32x32x16_bf16 v[16:31], v[96:99], v[112:115], v[16:31]
	s_waitcnt vmcnt(4)
	ds_write_b128 v212, v[178:181] offset:16384
	ds_write_b128 v213, v[182:185] offset:16384
	ds_write_b128 v214, v[186:189] offset:49152
	ds_write_b128 v215, v[190:193] offset:49152
	v_mfma_f32_32x32x16_bf16 v[16:31], v[100:103], v[116:119], v[16:31]
